# P1 projection queue: the claim atomic for the following unit is issued by the claiming wave at the start of the epilogue and consumed with a counted vmcnt(16), so neither the atomic round trip nor sto
# baseline (speedup 1.0000x reference)
.LBB0_227:
	v_readlane_b32 s2, v251, 14
	v_readlane_b32 s3, v251, 15
	s_cmp_lt_i32 s2, 2
	s_cselect_b64 s[2:3], -1, 0
	s_and_b64 s[0:1], s[2:3], s[0:1]
	s_andn2_b64 vcc, exec, s[0:1]
	s_cbranch_vccnz .LBB0_643
	s_mov_b32 s98, 0
	s_mov_b32 s99, 0
	v_readlane_b32 s0, v251, 19
	s_addk_i32 s0, 0xff84
	v_readlane_b32 s4, v251, 0
	s_cmp_lt_i32 s4, s0
	v_readlane_b32 s1, v251, 20
	v_readlane_b32 s5, v251, 1
	v_mbcnt_lo_u32_b32 v128, -1, 0
	v_mbcnt_hi_u32_b32 v128, -1, v128
	s_cbranch_scc1 .LBB0_271
	v_readlane_b32 s4, v251, 0
	s_sub_i32 s0, s4, s0
	s_lshl_b32 s10, s0, 3
	v_readlane_b32 s0, v251, 40
	s_add_i32 s10, s10, s0
	s_cmp_lt_u32 s10, 0x18000
	s_cselect_b64 s[6:7], -1, 0
	s_cmp_gt_u32 s10, 0x17fff
	v_readlane_b32 s5, v251, 1
	s_cbranch_scc1 .LBB0_233
	s_cmpk_gt_u32 s10, 0xffff
	s_cbranch_scc0 .LBB0_235
	s_lshl_b32 s1, s10, 5
	s_add_i32 s0, s10, 0xffff0000
	s_and_b32 s11, s1, 0x7e0
	s_lshl_b32 s1, s10, 1
	s_lshr_b32 s0, s0, 10
	s_waitcnt lgkmcnt(0)
	s_and_b32 s12, s1, 0x780
	s_mov_b32 s1, 0
	s_lshl_b64 s[8:9], s[0:1], 22
	s_lshl_b64 s[0:1], s[0:1], 24
	v_readlane_b32 s36, v251, 2
	v_readlane_b32 s37, v251, 3
	s_add_u32 s0, s36, s0
	s_addc_u32 s1, s37, s1
	s_lshl_b32 s4, s12, 13
	s_add_u32 s0, s0, s4
	s_addc_u32 s1, s1, 0
	s_lshl_b32 s4, s11, 2
	s_add_u32 s4, s0, s4
	v_readlane_b32 s16, v251, 10
	s_addc_u32 s5, s1, 0
	v_readlane_b32 s18, v251, 12
	v_readlane_b32 s19, v251, 13
	s_add_u32 s0, s18, s8
	s_addc_u32 s1, s19, s9
	s_lshl_b32 s8, s11, 11
	s_add_u32 s0, s0, s8
	s_addc_u32 s1, s1, 0
	s_add_u32 s0, s0, s12
	s_addc_u32 s1, s1, 0
	s_add_u32 s0, s0, 0x27900000
	v_readlane_b32 s38, v251, 4
	v_readlane_b32 s39, v251, 5
	v_readlane_b32 s40, v251, 6
	v_readlane_b32 s41, v251, 7
	v_readlane_b32 s42, v251, 8
	v_readlane_b32 s43, v251, 9
	v_readlane_b32 s17, v251, 11
	s_addc_u32 s1, s1, 0
	s_cbranch_execz .LBB0_236
	s_waitcnt lgkmcnt(0)
	s_mov_b32 s16, 0x44800000
	s_mov_b64 s[8:9], 0x800
	s_branch .LBB0_237

.LBB0_345:
	s_cmp_eq_u32 s98, 1
	s_cbranch_scc0 .Lq2_orig
	s_mov_b32 s98, 0
	s_waitcnt vmcnt(16)
	v_readfirstlane_b32 s31, v240
	s_and_b32 s30, s80, 1
	s_lshl_b32 s30, s30, 2
	s_add_i32 s30, s30, 0x24210
	v_mov_b32_e32 v0, s31
	v_mov_b32_e32 v1, s30
	s_mov_b64 s[100:101], exec
	s_mov_b64 exec, 1
	ds_write_b32 v1, v0
	s_mov_b64 exec, s[100:101]
	s_waitcnt lgkmcnt(0)
	s_branch .LBB0_350

.LBB0_361:
	s_cmp_gt_i32 s82, 7
	s_cbranch_scc1 .Lq2_nopre
	s_and_b64 vcc, exec, s[0:1]
	s_cbranch_vccnz .Lq2_nopre
	s_add_i32 s99, s51, s82
	s_and_b32 s99, s99, 7
	s_lshl_b32 s99, s99, 8
	s_mov_b64 s[100:101], exec
	s_mov_b64 exec, 1
	v_mov_b32_e32 v241, s99
	v_mov_b32_e32 v242, 1
	s_nop 0
	global_atomic_add v240, v241, v242, s[34:35] sc0
	s_mov_b64 exec, s[100:101]
	s_mov_b32 s98, 1
